# g7 + packed row-sum adds + scale-free conversion fast path
# baseline (speedup 1.0000x reference)
; template <bool FIRST> DEVI bool partialSM(f32x16& p0, f32x16& p1, float& m_reg, float& alpha) {
;     float pmax = p0[0];
; #pragma unroll
;     for (int r = 1; r < 16; ++r) pmax = fmaxf(pmax, p0[r]);
; #pragma unroll
;     for (int r = 0; r < 16; ++r) pmax = fmaxf(pmax, p1[r]);
;     { auto rr = __builtin_amdgcn_permlane32_swap(__float_as_uint(pmax), __float_as_uint(pmax), false, false);
;       pmax = fmaxf(__uint_as_float(rr[0]), __uint_as_float(rr[1])); }
;     if (FIRST) { m_reg = pmax; alpha = 1.f;
; #pragma unroll
;         for (int r = 0; r < 16; ++r) { p0[r] = __builtin_amdgcn_exp2f(p0[r] - pmax); p1[r] = p1[r] - pmax; }
;         return false;
;     } else if (__builtin_expect(__all(pmax <= ATT_THR), 1)) { alpha = 1.f;
; #pragma unroll
;         for (int r = 0; r < 16; ++r) p0[r] = __builtin_amdgcn_exp2f(p0[r]);
;         return false;
;     } else { const float d = fmaxf(pmax, 0.f); alpha = __builtin_amdgcn_exp2f(-d); m_reg += d;
; #pragma unroll
;         for (int r = 0; r < 16; ++r) { p0[r] = __builtin_amdgcn_exp2f(p0[r] - d); p1[r] = p1[r] - d; }
;         return true;
;     }
; }
; DEVI void finishSM(f32x16& p0, f32x16& p1, float alpha, float& l_reg, bf16x8& pa0, bf16x8& pa1, bf16x8& pa2, bf16x8& pa3) {
; #pragma unroll
;     for (int r = 0; r < 16; ++r) p1[r] = __builtin_amdgcn_exp2f(p1[r]);
;     f32x2 s2 = (f32x2){p0[0], p0[1]} + (f32x2){p1[0], p1[1]};
; #pragma unroll
;     for (int r = 2; r < 16; r += 2) s2 += (f32x2){p0[r], p0[r + 1]} + (f32x2){p1[r], p1[r + 1]};
;     float ps = s2[0] + s2[1];
;     { auto rr = __builtin_amdgcn_permlane32_swap(__float_as_uint(ps), __float_as_uint(ps), false, false);
;       ps = __uint_as_float(rr[0]) + __uint_as_float(rr[1]); }
;     l_reg = l_reg * alpha + ps;
;     ...
;     PK4(p0, 0, pa0); PK4(p0, 8, pa1); PK4(p1, 0, pa2); PK4(p1, 8, pa3);
;     ...
; }
; DEVI void qkt(f32x16& p0, f32x16& p1, const char* Kb, const bf16x8 (&qr)[6], int r32, int hi, const f32x16& cinit) {
; #pragma unroll
;     for (int d0 = 0; d0 < 6; ++d0) { const int cb = (d0 * 16 + hi * 8) * 2;
;         const bf16x8 k0 = *(const bf16x8*)(Kb + KSWZ(r32, cb)), k1 = *(const bf16x8*)(Kb + KSWZ(32 + r32, cb));
;         p0 = __builtin_amdgcn_mfma_f32_32x32x16_bf16(k0, qr[d0], d0 == 0 ? cinit : p0, 0, 0, 0);
;         p1 = __builtin_amdgcn_mfma_f32_32x32x16_bf16(k1, qr[d0], d0 == 0 ? cinit : p1, 0, 0, 0); }
; }
.LBB0_696:
	v_add_u32_e32 v174, s98, v204
	v_exp_f32_e32 v66, v66
	v_exp_f32_e32 v67, v67
	s_waitcnt lgkmcnt(1)
	v_mfma_f32_32x32x16_bf16 v[98:113], v[82:85], v[150:153], v[34:49]
	v_add_u32_e32 v82, s98, v184
	v_add_u32_e32 v83, s98, v185
	ds_read_b128 v[208:211], v82 offset:12288
	ds_read_b128 v[212:215], v82 offset:18432
	ds_read_b128 v[216:219], v83 offset:12288
	ds_read_b128 v[220:223], v83 offset:18432
	v_exp_f32_e32 v68, v68
	v_exp_f32_e32 v69, v69
	v_exp_f32_e32 v70, v70
	v_exp_f32_e32 v71, v71
	s_waitcnt lgkmcnt(4)
	v_mfma_f32_32x32x16_bf16 v[82:97], v[124:127], v[150:153], v[34:49]
	ds_read_b128 v[124:127], v174 offset:12288
	ds_read_b128 v[224:227], v174 offset:18432
	v_exp_f32_e32 v72, v72
	v_exp_f32_e32 v73, v73
	v_exp_f32_e32 v74, v74
	v_exp_f32_e32 v75, v75
	v_exp_f32_e32 v76, v76
	v_exp_f32_e32 v77, v77
	s_waitcnt lgkmcnt(5)
	v_mfma_f32_32x32x16_bf16 v[98:113], v[208:211], v[138:141], v[98:113]
	v_add_u32_e32 v174, s98, v205
	v_exp_f32_e32 v78, v78
	v_exp_f32_e32 v79, v79
	ds_read_b128 v[228:231], v174 offset:12288
	ds_read_b128 v[232:235], v174 offset:18432
	v_exp_f32_e32 v80, v80
	v_exp_f32_e32 v81, v81
	v_add_u32_e32 v174, s98, v206
	s_waitcnt lgkmcnt(6)
	v_mfma_f32_32x32x16_bf16 v[82:97], v[212:215], v[138:141], v[82:97]
	v_pk_add_f32 v[212:213], v[50:51], v[66:67]
	v_pk_add_f32 v[214:215], v[52:53], v[68:69]
	v_lshl_add_u32 v202, s89, 14, v115
	v_pk_add_f32 v[212:213], v[214:215], v[212:213]
	v_pk_add_f32 v[214:215], v[54:55], v[70:71]
	ds_read_b128 v[208:211], v174 offset:12288
	ds_read_b128 v[236:239], v174 offset:18432
	v_pk_add_f32 v[212:213], v[214:215], v[212:213]
	s_waitcnt lgkmcnt(7)
	v_mfma_f32_32x32x16_bf16 v[98:113], v[216:219], v[134:137], v[98:113]
	v_pk_add_f32 v[214:215], v[56:57], v[72:73]
	v_cvt_pk_bf16_f32 v50, v50, v51
	v_cvt_pk_bf16_f32 v51, v52, v53
	v_cvt_pk_bf16_f32 v52, v54, v55
	v_cvt_pk_bf16_f32 v53, v56, v57
	v_cvt_pk_bf16_f32 v54, v58, v59
	v_pk_add_f32 v[212:213], v[214:215], v[212:213]
	s_waitcnt lgkmcnt(6)
	v_mfma_f32_32x32x16_bf16 v[82:97], v[220:223], v[134:137], v[82:97]
	v_pk_add_f32 v[214:215], v[58:59], v[74:75]
	v_cvt_pk_bf16_f32 v55, v60, v61
	v_cvt_pk_bf16_f32 v56, v62, v63
	v_cvt_pk_bf16_f32 v57, v64, v65
	v_cvt_pk_bf16_f32 v58, v66, v67
	v_cvt_pk_bf16_f32 v59, v68, v69
	v_pk_add_f32 v[212:213], v[214:215], v[212:213]
	s_waitcnt lgkmcnt(5)
	v_mfma_f32_32x32x16_bf16 v[98:113], v[124:127], v[130:133], v[98:113]
	v_pk_add_f32 v[214:215], v[60:61], v[76:77]
	v_pk_add_f32 v[126:127], v[62:63], v[78:79]
	v_pk_add_f32 v[124:125], v[214:215], v[212:213]
	v_cvt_pk_bf16_f32 v60, v70, v71
	v_cvt_pk_bf16_f32 v61, v72, v73
	v_cvt_pk_bf16_f32 v62, v74, v75
	v_cvt_pk_bf16_f32 v63, v76, v77
	s_waitcnt lgkmcnt(4)
	v_mfma_f32_32x32x16_bf16 v[82:97], v[224:227], v[130:133], v[82:97]
	v_pk_add_f32 v[124:125], v[126:127], v[124:125]
	v_pk_add_f32 v[126:127], v[64:65], v[80:81]
	v_cvt_pk_bf16_f32 v64, v78, v79
	v_cvt_pk_bf16_f32 v65, v80, v81
	ds_read_b64_tr_b16 v[66:67], v202 offset:0
	ds_read_b64_tr_b16 v[68:69], v202 offset:0x400
	ds_read_b64_tr_b16 v[70:71], v202 offset:0x800
	s_waitcnt lgkmcnt(6)
	v_mfma_f32_32x32x16_bf16 v[98:113], v[228:231], v[146:149], v[98:113]
	ds_read_b64_tr_b16 v[72:73], v202 offset:0xc00
	ds_read_b64_tr_b16 v[74:75], v202 offset:0x1000
	ds_read_b64_tr_b16 v[76:77], v202 offset:0x1400
	ds_read_b64_tr_b16 v[78:79], v202 offset:0x1800
	ds_read_b64_tr_b16 v[80:81], v202 offset:0x1c00
	v_pk_add_f32 v[124:125], v[126:127], v[124:125]
	s_waitcnt lgkmcnt(10)
	v_mfma_f32_32x32x16_bf16 v[82:97], v[232:235], v[146:149], v[82:97]
	v_pk_add_f32 v[124:125], v[124:125], v[124:125] op_sel:[0,1] op_sel_hi:[1,0]
	s_nop 0
	v_mov_b32_e32 v125, v124
	s_nop 1
	v_permlane32_swap_b32_e32 v124, v125
	s_waitcnt lgkmcnt(9)
	v_mfma_f32_32x32x16_bf16 v[98:113], v[208:211], v[142:145], v[98:113]
	ds_read_b64_tr_b16 v[208:209], v202 offset:0x200
	ds_read_b64_tr_b16 v[210:211], v202 offset:0x600
	ds_read_b64_tr_b16 v[212:213], v202 offset:0xa00
	ds_read_b64_tr_b16 v[214:215], v202 offset:0xe00
	ds_read_b64_tr_b16 v[216:217], v202 offset:0x1200
	ds_read_b64_tr_b16 v[218:219], v202 offset:0x1600
	ds_read_b64_tr_b16 v[220:221], v202 offset:0x1a00
	s_waitcnt lgkmcnt(15)
	v_mfma_f32_32x32x16_bf16 v[82:97], v[236:239], v[142:145], v[82:97]
	ds_read_b64_tr_b16 v[222:223], v202 offset:0x1e00
	s_waitcnt lgkmcnt(14)
	v_mfma_f32_32x32x16_bf16 v[18:33], v[50:53], v[66:69], v[18:33]
	s_waitcnt lgkmcnt(12)
	v_mfma_f32_32x32x16_bf16 v[18:33], v[54:57], v[70:73], v[18:33]
	s_waitcnt lgkmcnt(10)
	v_mfma_f32_32x32x16_bf16 v[18:33], v[58:61], v[74:77], v[18:33]
	s_waitcnt lgkmcnt(8)
	v_mfma_f32_32x32x16_bf16 v[18:33], v[62:65], v[78:81], v[18:33]
	s_waitcnt lgkmcnt(6)
	v_mfma_f32_32x32x16_bf16 v[2:17], v[50:53], v[208:211], v[2:17]
	s_nop 4
	v_max_f32_e32 v249, v99, v99
	v_max_f32_e32 v250, v98, v98
	v_max_f32_e32 v249, v250, v249
	v_max3_f32 v249, v249, v100, v101
	v_max3_f32 v249, v249, v102, v103
	v_max3_f32 v251, v249, v104, v105
	v_max3_f32 v251, v251, v106, v107
	s_waitcnt lgkmcnt(4)
	v_exp_f32_e32 v50, v98
	v_exp_f32_e32 v51, v99
	v_exp_f32_e32 v52, v100
	v_exp_f32_e32 v53, v101
	v_mov_b64_e32 v[66:67], v[82:83]
	v_mov_b64_e32 v[68:69], v[84:85]
	v_mfma_f32_32x32x16_bf16 v[2:17], v[54:57], v[212:215], v[2:17]
	v_max3_f32 v251, v251, v108, v109
	v_max3_f32 v251, v251, v110, v111
	v_max3_f32 v251, v251, v112, v113
	v_max3_f32 v251, v251, v82, v83
	v_max3_f32 v251, v251, v84, v85
	v_max3_f32 v251, v251, v86, v87
	v_max3_f32 v251, v251, v88, v89
	s_waitcnt lgkmcnt(2)
	v_exp_f32_e32 v54, v102
	v_exp_f32_e32 v55, v103
	v_exp_f32_e32 v56, v104
	v_exp_f32_e32 v57, v105
	v_mov_b64_e32 v[70:71], v[86:87]
	v_mov_b64_e32 v[72:73], v[88:89]
	v_mfma_f32_32x32x16_bf16 v[2:17], v[58:61], v[216:219], v[2:17]
	v_max3_f32 v251, v251, v90, v91
	v_max3_f32 v251, v251, v92, v93
	v_max3_f32 v251, v251, v94, v95
	v_max3_f32 v251, v251, v96, v97
	v_mov_b32_e32 v252, v251
	s_nop 1
	v_permlane32_swap_b32_e32 v251, v252
	s_waitcnt lgkmcnt(0)
	v_exp_f32_e32 v58, v106
	v_exp_f32_e32 v59, v107
	v_exp_f32_e32 v60, v108
	v_exp_f32_e32 v61, v109
	v_mov_b64_e32 v[74:75], v[90:91]
	v_mov_b64_e32 v[76:77], v[92:93]
	v_mfma_f32_32x32x16_bf16 v[2:17], v[62:65], v[220:223], v[2:17]
	v_exp_f32_e32 v62, v110
	v_exp_f32_e32 v63, v111
	v_exp_f32_e32 v64, v112
	v_exp_f32_e32 v65, v113
	v_mov_b64_e32 v[78:79], v[94:95]
	v_mov_b64_e32 v[80:81], v[96:97]
	v_max_f32_e32 v252, v252, v252
	v_max_f32_e32 v251, v251, v251
	v_max_f32_e32 v126, v251, v252
	v_cmp_ge_f32_e32 vcc, s79, v126
	s_cmp_lg_u64 vcc, exec
	s_cselect_b64 s[6:7], -1, 0
	s_cbranch_scc1 .LBB0_705
	v_mov_b32_e32 v208, 1.0
	v_mov_b32_e32 v209, v203
	s_branch .LBB0_699

; #define VM0() asm volatile("s_waitcnt vmcnt(0)" ::: "memory")
; #define B_RESC(a, rare) do { if (rare) { if (hi == 0) al_l[r32] = (a); asm volatile("s_waitcnt lgkmcnt(0)" ::: "memory"); __builtin_amdgcn_wave_barrier(); \
;         _Pragma("unroll") for (int _d = 0; _d < 2; ++_d) _Pragma("unroll") for (int _r = 0; _r < 16; ++_r) o[_d][_r] *= al_l[crow(_r, hi)]; C_SPLAT(); } } while (0)
; DEVI void finishSM(f32x16& p0, f32x16& p1, float alpha, float& l_reg, bf16x8& pa0, bf16x8& pa1, bf16x8& pa2, bf16x8& pa3) {
; #pragma unroll
;     for (int r = 0; r < 16; ++r) p1[r] = __builtin_amdgcn_exp2f(p1[r]);
;     f32x2 s2 = (f32x2){p0[0], p0[1]} + (f32x2){p1[0], p1[1]};
; #pragma unroll
;     for (int r = 2; r < 16; r += 2) s2 += (f32x2){p0[r], p0[r + 1]} + (f32x2){p1[r], p1[r + 1]};
;     float ps = s2[0] + s2[1];
;     { auto rr = __builtin_amdgcn_permlane32_swap(__float_as_uint(ps), __float_as_uint(ps), false, false);
;       ps = __uint_as_float(rr[0]) + __uint_as_float(rr[1]); }
;     l_reg = l_reg * alpha + ps;
; DEVI void attn_unit8(const Params& p, char* smem, int unit, int l, int& cvs  , CvRun& crun) {
;     ...
;     B_DMA(0, 0); B_DMA(1, 1); VM0(); __syncthreads();
;     f32x16 cinit;
;     ...
;     { f32x16 z; _Pragma("unroll") for (int r = 0; r < 16; ++r) z[r] = 0.f;
;       qkt(pA0, pA1, K_lds, qr, r32, hi, z); } partialSM<true>(pA0, pA1, m_reg, alA); C_SPLAT();
;     int s0 = 0, s1 = 1, s2 = 2;
;     for (int T = 0; T + 1 < NTILE; ++T) {
;         const char* Kb = K_lds + s0 * 24576; const int vb = vb0 + s0 * 16384;
;         CvRegs cvr; cv_issue(p, l, cvs, lane, cvr, crun); cvs += (int)gridDim.x * 8;
;         qkt(pB0, pB1, Kb + 12288, qr, r32, hi, cinit);
;         finishSM(pA0, pA1, alA, l_reg, pa0, pa1, pa2, pa3);
;         pv_both(o[0], o[1], vb, pa0, pa1, pa2, pa3);
;         { const bool rr_ = partialSM<false>(pB0, pB1, m_reg, alB); B_RESC(alB, rr_); }
;         cv_finish(smem + 124928 + wid * 2304, lane, cvr);
;         if (cvr.live) asm volatile("s_waitcnt vmcnt(2)" ::: "memory"); else VM0();
;         __syncthreads();
;         if (T + 2 < NTILE) B_DMA(T + 2, s2);
;         qkt(pA0, pA1, K_lds + s1 * 24576, qr, r32, hi, cinit);
;         finishSM(pB0, pB1, alB, l_reg, pa0, pa1, pa2, pa3);
;         pv_both(o[0], o[1], vb + 8192, pa0, pa1, pa2, pa3);
;         { const bool rr_ = partialSM<false>(pA0, pA1, m_reg, alA); B_RESC(alA, rr_); }
.LBB0_702:
	s_mul_i32 s98, s2, 0x6000
	s_add_i32 s98, s96, s98
	s_lshl_b32 s99, s2, 14
	s_add_i32 s99, s97, s99
	s_mul_i32 s6, s61, 0x6000
	s_add_i32 s6, s6, 0
	v_add_u32_e32 v86, s6, v129
	v_lshl_add_u64 v[250:251], v[118:119], 0, s[12:13]
	s_mov_b32 m0, s98
	s_barrier
	ds_read_b128 v[82:85], v86
	ds_read_b128 v[210:213], v86 offset:6144
	global_load_lds_dwordx4 v[250:251], off
	v_exp_f32_e32 v66, v66
	s_waitcnt lgkmcnt(1)
	v_mfma_f32_32x32x16_bf16 v[98:113], v[82:85], v[150:153], v[34:49]
	v_add_u32_e32 v126, s6, v184
	v_lshl_add_u64 v[250:251], v[120:121], 0, s[12:13]
	s_add_i32 m0, s98, 0x2000
	v_exp_f32_e32 v67, v67
	v_exp_f32_e32 v68, v68
	global_load_lds_dwordx4 v[250:251], off
	v_exp_f32_e32 v69, v69
	v_exp_f32_e32 v70, v70
	v_exp_f32_e32 v71, v71
	v_exp_f32_e32 v72, v72
	s_waitcnt lgkmcnt(0)
	v_mfma_f32_32x32x16_bf16 v[82:97], v[210:213], v[150:153], v[34:49]
	ds_read_b128 v[210:213], v126
	ds_read_b128 v[214:217], v126 offset:6144
	v_add_u32_e32 v126, s6, v185
	v_lshl_add_u64 v[250:251], v[122:123], 0, s[12:13]
	s_add_i32 m0, s98, 0x4000
	v_exp_f32_e32 v73, v73
	v_exp_f32_e32 v74, v74
	global_load_lds_dwordx4 v[250:251], off
	v_exp_f32_e32 v75, v75
	v_exp_f32_e32 v76, v76
	v_exp_f32_e32 v77, v77
	s_waitcnt lgkmcnt(1)
	v_mfma_f32_32x32x16_bf16 v[98:113], v[210:213], v[138:141], v[98:113]
	s_mov_b32 m0, s99
	v_exp_f32_e32 v78, v78
	v_exp_f32_e32 v79, v79
	v_lshl_add_u64 v[250:251], v[116:117], 0, s[40:41]
	global_load_lds_dwordx4 v[116:117], off
	s_add_i32 m0, s99, 0x2000
	v_exp_f32_e32 v80, v80
	v_exp_f32_e32 v81, v81
	v_add_u32_e32 v174, 0x2000, v202
	global_load_lds_dwordx4 v[250:251], off
	s_waitcnt lgkmcnt(0)
	v_mfma_f32_32x32x16_bf16 v[82:97], v[214:217], v[138:141], v[82:97]
	ds_read_b128 v[210:213], v126
	ds_read_b128 v[214:217], v126 offset:6144
	v_add_u32_e32 v126, s6, v204
	s_waitcnt lgkmcnt(1)
	v_mfma_f32_32x32x16_bf16 v[98:113], v[210:213], v[134:137], v[98:113]
	ds_read_b128 v[210:213], v126
	ds_read_b128 v[218:221], v126 offset:6144
	v_add_u32_e32 v126, s6, v205
	s_waitcnt lgkmcnt(2)
	v_mfma_f32_32x32x16_bf16 v[82:97], v[214:217], v[134:137], v[82:97]
	ds_read_b128 v[214:217], v126
	ds_read_b128 v[222:225], v126 offset:6144
	v_add_u32_e32 v126, s6, v206
	ds_read_b128 v[226:229], v126
	ds_read_b128 v[230:233], v126 offset:6144
	v_pk_add_f32 v[126:127], v[50:51], v[66:67]
	v_cvt_pk_bf16_f32 v50, v50, v51
	v_cvt_pk_bf16_f32 v51, v52, v53
	s_waitcnt lgkmcnt(5)
	v_mfma_f32_32x32x16_bf16 v[98:113], v[210:213], v[130:133], v[98:113]
	v_pk_add_f32 v[210:211], v[52:53], v[68:69]
	v_cvt_pk_bf16_f32 v52, v54, v55
	v_cvt_pk_bf16_f32 v53, v56, v57
	v_pk_add_f32 v[126:127], v[210:211], v[126:127]
	v_pk_add_f32 v[210:211], v[54:55], v[70:71]
	v_cvt_pk_bf16_f32 v54, v58, v59
	s_waitcnt lgkmcnt(4)
	v_mfma_f32_32x32x16_bf16 v[82:97], v[218:221], v[130:133], v[82:97]
	v_pk_add_f32 v[126:127], v[210:211], v[126:127]
	v_pk_add_f32 v[210:211], v[56:57], v[72:73]
	v_cvt_pk_bf16_f32 v55, v60, v61
	v_cvt_pk_bf16_f32 v56, v62, v63
	v_cvt_pk_bf16_f32 v57, v64, v65
	v_pk_add_f32 v[126:127], v[210:211], v[126:127]
	v_pk_add_f32 v[210:211], v[58:59], v[74:75]
	v_cvt_pk_bf16_f32 v58, v66, v67
	v_cvt_pk_bf16_f32 v59, v68, v69
	s_waitcnt lgkmcnt(3)
	v_mfma_f32_32x32x16_bf16 v[98:113], v[214:217], v[146:149], v[98:113]
	v_pk_add_f32 v[126:127], v[210:211], v[126:127]
	v_pk_add_f32 v[210:211], v[60:61], v[76:77]
	v_cvt_pk_bf16_f32 v60, v70, v71
	v_cvt_pk_bf16_f32 v61, v72, v73
	v_pk_add_f32 v[126:127], v[210:211], v[126:127]
	v_pk_add_f32 v[210:211], v[62:63], v[78:79]
	v_cvt_pk_bf16_f32 v62, v74, v75
	v_cvt_pk_bf16_f32 v63, v76, v77
	s_waitcnt lgkmcnt(2)
; template <bool FIRST> DEVI bool partialSM(f32x16& p0, f32x16& p1, float& m_reg, float& alpha) {
;     float pmax = p0[0];
; #pragma unroll
;     for (int r = 1; r < 16; ++r) pmax = fmaxf(pmax, p0[r]);
; #pragma unroll
;     for (int r = 0; r < 16; ++r) pmax = fmaxf(pmax, p1[r]);
;     { auto rr = __builtin_amdgcn_permlane32_swap(__float_as_uint(pmax), __float_as_uint(pmax), false, false);
;       pmax = fmaxf(__uint_as_float(rr[0]), __uint_as_float(rr[1])); }
;     if (FIRST) { m_reg = pmax; alpha = 1.f;
; #pragma unroll
;         for (int r = 0; r < 16; ++r) { p0[r] = __builtin_amdgcn_exp2f(p0[r] - pmax); p1[r] = p1[r] - pmax; }
;         return false;
;     } else if (__builtin_expect(__all(pmax <= ATT_THR), 1)) { alpha = 1.f;
; #pragma unroll
;         for (int r = 0; r < 16; ++r) p0[r] = __builtin_amdgcn_exp2f(p0[r]);
;         return false;
;     } else { const float d = fmaxf(pmax, 0.f); alpha = __builtin_amdgcn_exp2f(-d); m_reg += d;
; #pragma unroll
;         for (int r = 0; r < 16; ++r) { p0[r] = __builtin_amdgcn_exp2f(p0[r] - d); p1[r] = p1[r] - d; }
;         return true;
;     }
; }
; DEVI void finishSM(f32x16& p0, f32x16& p1, float alpha, float& l_reg, bf16x8& pa0, bf16x8& pa1, bf16x8& pa2, bf16x8& pa3) {
; #pragma unroll
;     for (int r = 0; r < 16; ++r) p1[r] = __builtin_amdgcn_exp2f(p1[r]);
;     f32x2 s2 = (f32x2){p0[0], p0[1]} + (f32x2){p1[0], p1[1]};
; #pragma unroll
;     for (int r = 2; r < 16; r += 2) s2 += (f32x2){p0[r], p0[r + 1]} + (f32x2){p1[r], p1[r + 1]};
;     float ps = s2[0] + s2[1];
;     { auto rr = __builtin_amdgcn_permlane32_swap(__float_as_uint(ps), __float_as_uint(ps), false, false);
;       ps = __uint_as_float(rr[0]) + __uint_as_float(rr[1]); }
;     l_reg = l_reg * alpha + ps;
;     ...
;     PK4(p0, 0, pa0); PK4(p0, 8, pa1); PK4(p1, 0, pa2); PK4(p1, 8, pa3);
;     ...
; }
; DEVI void qkt(f32x16& p0, f32x16& p1, const char* Kb, const bf16x8 (&qr)[6], int r32, int hi, const f32x16& cinit) {
; #pragma unroll
;     for (int d0 = 0; d0 < 6; ++d0) { const int cb = (d0 * 16 + hi * 8) * 2;
;         const bf16x8 k0 = *(const bf16x8*)(Kb + KSWZ(r32, cb)), k1 = *(const bf16x8*)(Kb + KSWZ(32 + r32, cb));
;         p0 = __builtin_amdgcn_mfma_f32_32x32x16_bf16(k0, qr[d0], d0 == 0 ? cinit : p0, 0, 0, 0);
;         p1 = __builtin_amdgcn_mfma_f32_32x32x16_bf16(k1, qr[d0], d0 == 0 ? cinit : p1, 0, 0, 0); }
; }
	v_mfma_f32_32x32x16_bf16 v[82:97], v[222:225], v[146:149], v[82:97]
	v_pk_add_f32 v[126:127], v[210:211], v[126:127]
	v_pk_add_f32 v[210:211], v[64:65], v[80:81]
	v_cvt_pk_bf16_f32 v64, v78, v79
	v_cvt_pk_bf16_f32 v65, v80, v81
	ds_read_b64_tr_b16 v[66:67], v174 offset:0
	ds_read_b64_tr_b16 v[68:69], v174 offset:0x400
	ds_read_b64_tr_b16 v[70:71], v174 offset:0x800
	ds_read_b64_tr_b16 v[72:73], v174 offset:0xc00
	ds_read_b64_tr_b16 v[74:75], v174 offset:0x1000
	ds_read_b64_tr_b16 v[76:77], v174 offset:0x1400
	ds_read_b64_tr_b16 v[78:79], v174 offset:0x1800
	ds_read_b64_tr_b16 v[80:81], v174 offset:0x1c00
	v_pk_add_f32 v[126:127], v[210:211], v[126:127]
	ds_read_b64_tr_b16 v[210:211], v174 offset:0x200
	ds_read_b64_tr_b16 v[212:213], v174 offset:0x600
	ds_read_b64_tr_b16 v[214:215], v174 offset:0xa00
	s_waitcnt lgkmcnt(12)
	v_mfma_f32_32x32x16_bf16 v[98:113], v[226:229], v[142:145], v[98:113]
	ds_read_b64_tr_b16 v[216:217], v174 offset:0xe00
	ds_read_b64_tr_b16 v[218:219], v174 offset:0x1200
	ds_read_b64_tr_b16 v[220:221], v174 offset:0x1600
	ds_read_b64_tr_b16 v[222:223], v174 offset:0x1a00
	ds_read_b64_tr_b16 v[224:225], v174 offset:0x1e00
	v_pk_add_f32 v[126:127], v[126:127], v[126:127] op_sel:[0,1] op_sel_hi:[1,0]
	s_waitcnt lgkmcnt(15)
	v_mfma_f32_32x32x16_bf16 v[82:97], v[230:233], v[142:145], v[82:97]
	v_mov_b32_e32 v127, v126
	s_nop 1
	v_permlane32_swap_b32_e32 v126, v127
	s_waitcnt lgkmcnt(14)
	v_mfma_f32_32x32x16_bf16 v[18:33], v[50:53], v[66:69], v[18:33]
	s_waitcnt lgkmcnt(12)
	v_mfma_f32_32x32x16_bf16 v[18:33], v[54:57], v[70:73], v[18:33]
	s_waitcnt lgkmcnt(10)
	v_mfma_f32_32x32x16_bf16 v[18:33], v[58:61], v[74:77], v[18:33]
	s_waitcnt lgkmcnt(8)
	v_mfma_f32_32x32x16_bf16 v[18:33], v[62:65], v[78:81], v[18:33]
	s_waitcnt lgkmcnt(6)
	v_mfma_f32_32x32x16_bf16 v[2:17], v[50:53], v[210:213], v[2:17]
	s_nop 0
	v_max_f32_e32 v249, v99, v99
	v_max_f32_e32 v250, v98, v98
	v_max_f32_e32 v249, v250, v249
	v_max3_f32 v249, v249, v100, v101
	v_max3_f32 v249, v249, v102, v103
	v_max3_f32 v251, v249, v104, v105
	v_max3_f32 v251, v251, v106, v107
	s_waitcnt lgkmcnt(4)
	v_exp_f32_e32 v50, v98
	v_exp_f32_e32 v51, v99
	v_exp_f32_e32 v52, v100
	v_exp_f32_e32 v53, v101
	v_mov_b64_e32 v[66:67], v[82:83]
	v_mov_b64_e32 v[68:69], v[84:85]
	v_mfma_f32_32x32x16_bf16 v[2:17], v[54:57], v[214:217], v[2:17]
	v_max3_f32 v251, v251, v108, v109
	v_max3_f32 v251, v251, v110, v111
	v_max3_f32 v251, v251, v112, v113
	v_max3_f32 v251, v251, v82, v83
	v_max3_f32 v251, v251, v84, v85
	v_max3_f32 v251, v251, v86, v87
	v_max3_f32 v251, v251, v88, v89
	s_waitcnt lgkmcnt(2)
	v_exp_f32_e32 v54, v102
	v_exp_f32_e32 v55, v103
	v_exp_f32_e32 v56, v104
	v_exp_f32_e32 v57, v105
	v_mov_b64_e32 v[70:71], v[86:87]
	v_mov_b64_e32 v[72:73], v[88:89]
	v_mfma_f32_32x32x16_bf16 v[2:17], v[58:61], v[218:221], v[2:17]
	v_max3_f32 v251, v251, v90, v91
	v_max3_f32 v251, v251, v92, v93
	v_max3_f32 v251, v251, v94, v95
	v_max3_f32 v251, v251, v96, v97
	v_mov_b32_e32 v252, v251
	s_nop 1
	v_permlane32_swap_b32_e32 v251, v252
	s_waitcnt lgkmcnt(0)
	v_exp_f32_e32 v58, v106
	v_exp_f32_e32 v59, v107
	v_exp_f32_e32 v60, v108
	v_exp_f32_e32 v61, v109
	v_mov_b64_e32 v[74:75], v[90:91]
	v_mov_b64_e32 v[76:77], v[92:93]
	v_mfma_f32_32x32x16_bf16 v[2:17], v[62:65], v[222:225], v[2:17]
	v_exp_f32_e32 v62, v110
	v_exp_f32_e32 v63, v111
	v_exp_f32_e32 v64, v112
	v_exp_f32_e32 v65, v113
	v_mov_b64_e32 v[78:79], v[94:95]
	v_mov_b64_e32 v[80:81], v[96:97]
	v_max_f32_e32 v252, v252, v252
	v_max_f32_e32 v251, v251, v251
	v_max_f32_e32 v174, v251, v252
	v_cmp_ge_f32_e32 vcc, s79, v174
	s_cmp_lg_u64 vcc, exec
	s_cselect_b64 s[6:7], -1, 0
	s_cbranch_scc1 .LBB0_711
	v_mov_b32_e32 v202, 1.0
	v_mov_b32_e32 v203, v209
	s_branch .LBB0_716

; DEVI unsigned cvt_pk_bf16(float lo, float hi) { unsigned r; asm volatile("v_cvt_pk_bf16_f32 %0, %1, %2" : "=v"(r) : "v"(lo), "v"(hi)); return r; }
; DEVI void cv_finish(char* img  , int lane, const CvRegs& R) {
;     if (!R.live) return;
;     const int n4 = (lane & 7) * 4, kq = lane >> 3;
;     const float sc = R.c.perm ? 16.f : 1.f;
; #pragma unroll
;     for (int c = 0; c < 4; ++c) { *(unsigned*)(img + (n4 + c) * 68 + (2 * kq) * 2) = cvt_pk_bf16(R.a0[c] * sc, R.b0[c] * sc); *(unsigned*)(img + (n4 + c) * 68 + (2 * kq + 16) * 2) = cvt_pk_bf16(R.a1[c] * sc, R.b1[c] * sc); }
;     asm volatile("" ::: "memory"); __builtin_amdgcn_wave_barrier();
;     const int n = lane >> 1, half = lane & 1; u32x4 w0, w1;
; #pragma unroll
;     for (int j = 0; j < 4; ++j) { w0[j] = *(const unsigned*)(img + n * 68 + half * 32 + j * 4); w1[j] = *(const unsigned*)(img + n * 68 + half * 32 + 16 + j * 4); }
;     const int row = R.c.perm ? R.c.r0 + 128 * ((n >> 3) & 1) + 16 * ((n >> 2) & 1) + 4 * (n >> 4) + (n & 3) : R.c.r0 + 128 * ((n >> 2) & 1) + 4 * (n >> 3) + (n & 3);
;     bf16_t* d = R.c.dst + (size_t)row * R.c.K + R.c.k0 + half * 16;
;     __builtin_nontemporal_store(w0, (u32x4*)d); __builtin_nontemporal_store(w1, (u32x4*)(d + 8));
;     asm volatile("" ::: "memory"); __builtin_amdgcn_wave_barrier();
; }
.LBB0_710:
	s_cmp_eq_u32 s95, 0
	s_cselect_b64 vcc, -1, 0
	s_waitcnt vmcnt(0)
	s_cbranch_scc0 .Lmy_cvs_a
	v_add_u32_e32 v84, v200, v201
	v_cvt_pk_bf16_f32 v83, v154, v158
	v_cvt_pk_bf16_f32 v85, v162, v166
	ds_write2_b32 v84, v83, v85 offset0:0 offset1:8
	v_cvt_pk_bf16_f32 v83, v155, v159
	v_cvt_pk_bf16_f32 v85, v163, v167
	ds_write2_b32 v84, v83, v85 offset0:17 offset1:25
	v_cvt_pk_bf16_f32 v83, v156, v160
	v_cvt_pk_bf16_f32 v85, v164, v168
	ds_write2_b32 v84, v83, v85 offset0:34 offset1:42
	v_cvt_pk_bf16_f32 v83, v157, v161
	v_cvt_pk_bf16_f32 v85, v165, v169
	ds_write2_b32 v84, v83, v85 offset0:51 offset1:59
	v_add_u32_e32 v84, v198, v199
	v_or_b32_e32 v90, v197, v195
	s_branch .Lmy_cvj_a
.Lmy_cvs_a:
	v_cndmask_b32_e64 v82, v181, 1.0, vcc
	v_mul_f32_e32 v83, v82, v154
	v_mul_f32_e32 v84, v82, v158
	v_cvt_pk_bf16_f32 v83, v83, v84
	v_add_u32_e32 v84, v200, v201
	ds_write_b32 v84, v83
	v_mul_f32_e32 v83, v82, v162
	v_mul_f32_e32 v85, v82, v166
	v_cvt_pk_bf16_f32 v83, v83, v85
	ds_write_b32 v84, v83 offset:32
	v_mul_f32_e32 v83, v82, v155
	v_mul_f32_e32 v85, v82, v159
	v_cvt_pk_bf16_f32 v83, v83, v85
	ds_write_b32 v84, v83 offset:68
	v_mul_f32_e32 v83, v82, v163
	v_mul_f32_e32 v85, v82, v167
	v_cvt_pk_bf16_f32 v83, v83, v85
	ds_write_b32 v84, v83 offset:100
	v_mul_f32_e32 v83, v82, v156
	v_mul_f32_e32 v85, v82, v160
	v_cvt_pk_bf16_f32 v83, v83, v85
	ds_write_b32 v84, v83 offset:136
	v_mul_f32_e32 v83, v82, v164
	v_mul_f32_e32 v85, v82, v168
	v_cvt_pk_bf16_f32 v83, v83, v85
	ds_write_b32 v84, v83 offset:168
	v_mul_f32_e32 v83, v82, v157
	v_mul_f32_e32 v85, v82, v161
	v_cvt_pk_bf16_f32 v83, v83, v85
	ds_write_b32 v84, v83 offset:204
	v_mul_f32_e32 v83, v82, v165
	v_mul_f32_e32 v82, v82, v169
	v_cndmask_b32_e32 v90, v196, v197, vcc
	v_cvt_pk_bf16_f32 v82, v83, v82
	ds_write_b32 v84, v82 offset:236
	v_add_u32_e32 v84, v198, v199
	v_or_b32_e32 v90, v90, v195
.Lmy_cvj_a:
	ds_read2_b32 v[82:83], v84 offset1:1
	ds_read2_b32 v[86:87], v84 offset0:4 offset1:5
	ds_read2_b32 v[88:89], v84 offset0:6 offset1:7
	ds_read2_b32 v[84:85], v84 offset0:2 offset1:3
	v_add_u32_e32 v90, s8, v90
	v_mad_i64_i32 v[90:91], s[6:7], v90, s94, 0
	v_lshl_add_u64 v[90:91], v[90:91], 1, v[182:183]
	s_ashr_i32 s11, s10, 31
	v_lshl_add_u64 v[90:91], s[10:11], 1, v[90:91]
	v_lshlrev_b32_e32 v174, 1, v180
	v_lshl_add_u64 v[90:91], v[90:91], 0, v[174:175]
	s_waitcnt lgkmcnt(0)
	global_store_dwordx4 v[90:91], v[82:85], off nt
	global_store_dwordx4 v[90:91], v[86:89], off offset:16 nt
	s_waitcnt vmcnt(2)
	s_cbranch_execz .LBB0_701
	s_branch .LBB0_702

; template <bool FIRST> DEVI bool partialSM(f32x16& p0, f32x16& p1, float& m_reg, float& alpha) {
;     float pmax = p0[0];
; #pragma unroll
;     for (int r = 1; r < 16; ++r) pmax = fmaxf(pmax, p0[r]);
; #pragma unroll
;     for (int r = 0; r < 16; ++r) pmax = fmaxf(pmax, p1[r]);
;     { auto rr = __builtin_amdgcn_permlane32_swap(__float_as_uint(pmax), __float_as_uint(pmax), false, false);
;       pmax = fmaxf(__uint_as_float(rr[0]), __uint_as_float(rr[1])); }
;     if (FIRST) { m_reg = pmax; alpha = 1.f;
; #pragma unroll
;         for (int r = 0; r < 16; ++r) { p0[r] = __builtin_amdgcn_exp2f(p0[r] - pmax); p1[r] = p1[r] - pmax; }
;         return false;
;     } else if (__builtin_expect(__all(pmax <= ATT_THR), 1)) { alpha = 1.f;
; #pragma unroll
;         for (int r = 0; r < 16; ++r) p0[r] = __builtin_amdgcn_exp2f(p0[r]);
;         return false;
;     } else { const float d = fmaxf(pmax, 0.f); alpha = __builtin_amdgcn_exp2f(-d); m_reg += d;
; #pragma unroll
;         for (int r = 0; r < 16; ++r) { p0[r] = __builtin_amdgcn_exp2f(p0[r] - d); p1[r] = p1[r] - d; }
;         return true;
;     }
; }
; DEVI void finishSM(f32x16& p0, f32x16& p1, float alpha, float& l_reg, bf16x8& pa0, bf16x8& pa1, bf16x8& pa2, bf16x8& pa3) {
; #pragma unroll
;     for (int r = 0; r < 16; ++r) p1[r] = __builtin_amdgcn_exp2f(p1[r]);
;     f32x2 s2 = (f32x2){p0[0], p0[1]} + (f32x2){p1[0], p1[1]};
; #pragma unroll
;     for (int r = 2; r < 16; r += 2) s2 += (f32x2){p0[r], p0[r + 1]} + (f32x2){p1[r], p1[r + 1]};
;     float ps = s2[0] + s2[1];
;     { auto rr = __builtin_amdgcn_permlane32_swap(__float_as_uint(ps), __float_as_uint(ps), false, false);
;       ps = __uint_as_float(rr[0]) + __uint_as_float(rr[1]); }
;     l_reg = l_reg * alpha + ps;
;     ...
;     PK4(p0, 0, pa0); PK4(p0, 8, pa1); PK4(p1, 0, pa2); PK4(p1, 8, pa3);
;     ...
; }
; DEVI void qkt(f32x16& p0, f32x16& p1, const char* Kb, const bf16x8 (&qr)[6], int r32, int hi, const f32x16& cinit) {
; #pragma unroll
;     for (int d0 = 0; d0 < 6; ++d0) { const int cb = (d0 * 16 + hi * 8) * 2;
;         const bf16x8 k0 = *(const bf16x8*)(Kb + KSWZ(r32, cb)), k1 = *(const bf16x8*)(Kb + KSWZ(32 + r32, cb));
;         p0 = __builtin_amdgcn_mfma_f32_32x32x16_bf16(k0, qr[d0], d0 == 0 ? cinit : p0, 0, 0, 0);
;         p1 = __builtin_amdgcn_mfma_f32_32x32x16_bf16(k1, qr[d0], d0 == 0 ? cinit : p1, 0, 0, 0); }
; }
.LBB0_2260:
	v_add_u32_e32 v174, s98, v205
	v_exp_f32_e32 v66, v66
	v_exp_f32_e32 v67, v67
	s_waitcnt lgkmcnt(1)
	v_mfma_f32_32x32x16_bf16 v[98:113], v[82:85], v[150:153], v[34:49]
	v_add_u32_e32 v82, s98, v184
	v_add_u32_e32 v83, s98, v185
	ds_read_b128 v[210:213], v82 offset:12288
	ds_read_b128 v[214:217], v82 offset:18432
	ds_read_b128 v[218:221], v83 offset:12288
	ds_read_b128 v[222:225], v83 offset:18432
	v_exp_f32_e32 v68, v68
	v_exp_f32_e32 v69, v69
	v_exp_f32_e32 v70, v70
	v_exp_f32_e32 v71, v71
	s_waitcnt lgkmcnt(4)
	v_mfma_f32_32x32x16_bf16 v[82:97], v[124:127], v[150:153], v[34:49]
	ds_read_b128 v[124:127], v174 offset:12288
	ds_read_b128 v[226:229], v174 offset:18432
	v_exp_f32_e32 v72, v72
	v_exp_f32_e32 v73, v73
	v_exp_f32_e32 v74, v74
	v_exp_f32_e32 v75, v75
	v_exp_f32_e32 v76, v76
	v_exp_f32_e32 v77, v77
	s_waitcnt lgkmcnt(5)
	v_mfma_f32_32x32x16_bf16 v[98:113], v[210:213], v[138:141], v[98:113]
	v_add_u32_e32 v174, s98, v206
	v_exp_f32_e32 v78, v78
	v_exp_f32_e32 v79, v79
	ds_read_b128 v[230:233], v174 offset:12288
	ds_read_b128 v[234:237], v174 offset:18432
	v_exp_f32_e32 v80, v80
	v_exp_f32_e32 v81, v81
	v_add_u32_e32 v174, s98, v207
	s_waitcnt lgkmcnt(6)
	v_mfma_f32_32x32x16_bf16 v[82:97], v[214:217], v[138:141], v[82:97]
	v_pk_add_f32 v[214:215], v[50:51], v[66:67]
	v_pk_add_f32 v[216:217], v[52:53], v[68:69]
	v_lshl_add_u32 v203, s71, 14, v115
	v_pk_add_f32 v[214:215], v[216:217], v[214:215]
	v_pk_add_f32 v[216:217], v[54:55], v[70:71]
	ds_read_b128 v[210:213], v174 offset:12288
	ds_read_b128 v[238:241], v174 offset:18432
	v_pk_add_f32 v[214:215], v[216:217], v[214:215]
	s_waitcnt lgkmcnt(7)
	v_mfma_f32_32x32x16_bf16 v[98:113], v[218:221], v[134:137], v[98:113]
	v_pk_add_f32 v[216:217], v[56:57], v[72:73]
	v_cvt_pk_bf16_f32 v50, v50, v51
	v_cvt_pk_bf16_f32 v51, v52, v53
	v_cvt_pk_bf16_f32 v52, v54, v55
	v_cvt_pk_bf16_f32 v53, v56, v57
	v_cvt_pk_bf16_f32 v54, v58, v59
	v_pk_add_f32 v[214:215], v[216:217], v[214:215]
	s_waitcnt lgkmcnt(6)
	v_mfma_f32_32x32x16_bf16 v[82:97], v[222:225], v[134:137], v[82:97]
	v_pk_add_f32 v[216:217], v[58:59], v[74:75]
	v_cvt_pk_bf16_f32 v55, v60, v61
	v_cvt_pk_bf16_f32 v56, v62, v63
	v_cvt_pk_bf16_f32 v57, v64, v65
	v_cvt_pk_bf16_f32 v58, v66, v67
	v_cvt_pk_bf16_f32 v59, v68, v69
	v_pk_add_f32 v[214:215], v[216:217], v[214:215]
	s_waitcnt lgkmcnt(5)
	v_mfma_f32_32x32x16_bf16 v[98:113], v[124:127], v[130:133], v[98:113]
	v_pk_add_f32 v[216:217], v[60:61], v[76:77]
	v_pk_add_f32 v[126:127], v[62:63], v[78:79]
	v_pk_add_f32 v[124:125], v[216:217], v[214:215]
	v_cvt_pk_bf16_f32 v60, v70, v71
	v_cvt_pk_bf16_f32 v61, v72, v73
	v_cvt_pk_bf16_f32 v62, v74, v75
	v_cvt_pk_bf16_f32 v63, v76, v77
	s_waitcnt lgkmcnt(4)
	v_mfma_f32_32x32x16_bf16 v[82:97], v[226:229], v[130:133], v[82:97]
	v_pk_add_f32 v[124:125], v[126:127], v[124:125]
	v_pk_add_f32 v[126:127], v[64:65], v[80:81]
	v_cvt_pk_bf16_f32 v64, v78, v79
	v_cvt_pk_bf16_f32 v65, v80, v81
	ds_read_b64_tr_b16 v[66:67], v203 offset:0
	ds_read_b64_tr_b16 v[68:69], v203 offset:0x400
	ds_read_b64_tr_b16 v[70:71], v203 offset:0x800
	s_waitcnt lgkmcnt(6)
	v_mfma_f32_32x32x16_bf16 v[98:113], v[230:233], v[146:149], v[98:113]
	ds_read_b64_tr_b16 v[72:73], v203 offset:0xc00
	ds_read_b64_tr_b16 v[74:75], v203 offset:0x1000
	ds_read_b64_tr_b16 v[76:77], v203 offset:0x1400
	ds_read_b64_tr_b16 v[78:79], v203 offset:0x1800
	ds_read_b64_tr_b16 v[80:81], v203 offset:0x1c00
	v_pk_add_f32 v[124:125], v[126:127], v[124:125]
	s_waitcnt lgkmcnt(10)
	v_mfma_f32_32x32x16_bf16 v[82:97], v[234:237], v[146:149], v[82:97]
	v_pk_add_f32 v[124:125], v[124:125], v[124:125] op_sel:[0,1] op_sel_hi:[1,0]
	s_nop 0
	v_mov_b32_e32 v125, v124
	s_nop 1
	v_permlane32_swap_b32_e32 v124, v125
	s_waitcnt lgkmcnt(9)
	v_mfma_f32_32x32x16_bf16 v[98:113], v[210:213], v[142:145], v[98:113]
	ds_read_b64_tr_b16 v[210:211], v203 offset:0x200
	ds_read_b64_tr_b16 v[212:213], v203 offset:0x600
	ds_read_b64_tr_b16 v[214:215], v203 offset:0xa00
	ds_read_b64_tr_b16 v[216:217], v203 offset:0xe00
	ds_read_b64_tr_b16 v[218:219], v203 offset:0x1200
	ds_read_b64_tr_b16 v[220:221], v203 offset:0x1600
	ds_read_b64_tr_b16 v[222:223], v203 offset:0x1a00
	s_waitcnt lgkmcnt(15)
	v_mfma_f32_32x32x16_bf16 v[82:97], v[238:241], v[142:145], v[82:97]
	ds_read_b64_tr_b16 v[224:225], v203 offset:0x1e00
	s_waitcnt lgkmcnt(14)
	v_mfma_f32_32x32x16_bf16 v[18:33], v[50:53], v[66:69], v[18:33]
	s_waitcnt lgkmcnt(12)
	v_mfma_f32_32x32x16_bf16 v[18:33], v[54:57], v[70:73], v[18:33]
	s_waitcnt lgkmcnt(10)
	v_mfma_f32_32x32x16_bf16 v[18:33], v[58:61], v[74:77], v[18:33]
	s_waitcnt lgkmcnt(8)
	v_mfma_f32_32x32x16_bf16 v[18:33], v[62:65], v[78:81], v[18:33]
	s_waitcnt lgkmcnt(6)
	v_mfma_f32_32x32x16_bf16 v[2:17], v[50:53], v[210:213], v[2:17]
	s_nop 4
	v_max_f32_e32 v249, v99, v99
	v_max_f32_e32 v250, v98, v98
	v_max_f32_e32 v249, v250, v249
	v_max3_f32 v249, v249, v100, v101
	v_max3_f32 v249, v249, v102, v103
	v_max3_f32 v251, v249, v104, v105
	v_max3_f32 v251, v251, v106, v107
	s_waitcnt lgkmcnt(4)
	v_exp_f32_e32 v50, v98
	v_exp_f32_e32 v51, v99
	v_exp_f32_e32 v52, v100
	v_exp_f32_e32 v53, v101
	v_mov_b64_e32 v[66:67], v[82:83]
	v_mov_b64_e32 v[68:69], v[84:85]
	v_mfma_f32_32x32x16_bf16 v[2:17], v[54:57], v[214:217], v[2:17]
	v_max3_f32 v251, v251, v108, v109
	v_max3_f32 v251, v251, v110, v111
	v_max3_f32 v251, v251, v112, v113
	v_max3_f32 v251, v251, v82, v83
	v_max3_f32 v251, v251, v84, v85
	v_max3_f32 v251, v251, v86, v87
	v_max3_f32 v251, v251, v88, v89
	s_waitcnt lgkmcnt(2)
	v_exp_f32_e32 v54, v102
	v_exp_f32_e32 v55, v103
	v_exp_f32_e32 v56, v104
	v_exp_f32_e32 v57, v105
	v_mov_b64_e32 v[70:71], v[86:87]
	v_mov_b64_e32 v[72:73], v[88:89]
	v_mfma_f32_32x32x16_bf16 v[2:17], v[58:61], v[218:221], v[2:17]
	v_max3_f32 v251, v251, v90, v91
	v_max3_f32 v251, v251, v92, v93
	v_max3_f32 v251, v251, v94, v95
	v_max3_f32 v251, v251, v96, v97
	v_mov_b32_e32 v252, v251
	s_nop 1
	v_permlane32_swap_b32_e32 v251, v252
	s_waitcnt lgkmcnt(0)
	v_exp_f32_e32 v58, v106
	v_exp_f32_e32 v59, v107
	v_exp_f32_e32 v60, v108
	v_exp_f32_e32 v61, v109
	v_mov_b64_e32 v[74:75], v[90:91]
	v_mov_b64_e32 v[76:77], v[92:93]
	v_mfma_f32_32x32x16_bf16 v[2:17], v[62:65], v[222:225], v[2:17]
	v_exp_f32_e32 v62, v110
	v_exp_f32_e32 v63, v111
	v_exp_f32_e32 v64, v112
	v_exp_f32_e32 v65, v113
	v_mov_b64_e32 v[78:79], v[94:95]
	v_mov_b64_e32 v[80:81], v[96:97]
	v_max_f32_e32 v252, v252, v252
	v_max_f32_e32 v251, v251, v251
	v_max_f32_e32 v126, v251, v252
	v_cmp_ge_f32_e32 vcc, s80, v126
	s_cmp_lg_u64 vcc, exec
	s_cselect_b64 s[6:7], -1, 0
	s_cbranch_scc1 .LBB0_2269
	v_mov_b32_e32 v209, 1.0
	v_mov_b32_e32 v210, v204
	s_branch .LBB0_2263

; #define PK4(P, BASE, OUT) do { u32x4 w = {cvt_pk_bf16(P[BASE + 0], P[BASE + 1]), cvt_pk_bf16(P[BASE + 2], P[BASE + 3]), cvt_pk_bf16(P[BASE + 4], P[BASE + 5]), cvt_pk_bf16(P[BASE + 6], P[BASE + 7])}; \
;     OUT = *reinterpret_cast<bf16x8*>(&w); } while (0)
; DEVI void finishSM(f32x16& p0, f32x16& p1, float alpha, float& l_reg, bf16x8& pa0, bf16x8& pa1, bf16x8& pa2, bf16x8& pa3) {
; #pragma unroll
;     for (int r = 0; r < 16; ++r) p1[r] = __builtin_amdgcn_exp2f(p1[r]);
;     f32x2 s2 = (f32x2){p0[0], p0[1]} + (f32x2){p1[0], p1[1]};
; #pragma unroll
;     for (int r = 2; r < 16; r += 2) s2 += (f32x2){p0[r], p0[r + 1]} + (f32x2){p1[r], p1[r + 1]};
;     float ps = s2[0] + s2[1];
;     { auto rr = __builtin_amdgcn_permlane32_swap(__float_as_uint(ps), __float_as_uint(ps), false, false);
;       ps = __uint_as_float(rr[0]) + __uint_as_float(rr[1]); }
;     l_reg = l_reg * alpha + ps;
;     ...
;     PK4(p0, 0, pa0); PK4(p0, 8, pa1); PK4(p1, 0, pa2); PK4(p1, 8, pa3);
;     ...
; }
; DEVI void qkt(f32x16& p0, f32x16& p1, const char* Kb, const bf16x8 (&qr)[6], int r32, int hi, const f32x16& cinit) {
; #pragma unroll
;     for (int d0 = 0; d0 < 6; ++d0) { const int cb = (d0 * 16 + hi * 8) * 2;
;         const bf16x8 k0 = *(const bf16x8*)(Kb + KSWZ(r32, cb)), k1 = *(const bf16x8*)(Kb + KSWZ(32 + r32, cb));
;         p0 = __builtin_amdgcn_mfma_f32_32x32x16_bf16(k0, qr[d0], d0 == 0 ? cinit : p0, 0, 0, 0);
;         p1 = __builtin_amdgcn_mfma_f32_32x32x16_bf16(k1, qr[d0], d0 == 0 ? cinit : p1, 0, 0, 0); }
; }
.LBB0_2266:
	s_mul_i32 s98, s61, 0x6000
	s_add_i32 s98, s96, s98
	s_lshl_b32 s99, s61, 14
	s_add_i32 s99, s97, s99
	s_mul_i32 s6, s2, 0x6000
	s_add_i32 s6, s6, 0
	v_add_u32_e32 v86, s6, v129
	v_lshl_add_u64 v[250:251], v[118:119], 0, s[12:13]
	s_mov_b32 m0, s98
	s_barrier
	ds_read_b128 v[82:85], v86
	ds_read_b128 v[212:215], v86 offset:6144
	global_load_lds_dwordx4 v[250:251], off
	v_exp_f32_e32 v66, v66
	s_waitcnt lgkmcnt(1)
	v_mfma_f32_32x32x16_bf16 v[98:113], v[82:85], v[150:153], v[34:49]
	v_add_u32_e32 v126, s6, v184
	v_lshl_add_u64 v[250:251], v[120:121], 0, s[12:13]
	s_add_i32 m0, s98, 0x2000
	v_exp_f32_e32 v67, v67
	v_exp_f32_e32 v68, v68
	global_load_lds_dwordx4 v[250:251], off
	v_exp_f32_e32 v69, v69
	v_exp_f32_e32 v70, v70
	v_exp_f32_e32 v71, v71
	v_exp_f32_e32 v72, v72
	s_waitcnt lgkmcnt(0)
	v_mfma_f32_32x32x16_bf16 v[82:97], v[212:215], v[150:153], v[34:49]
	ds_read_b128 v[212:215], v126
	ds_read_b128 v[216:219], v126 offset:6144
	v_add_u32_e32 v126, s6, v185
	v_lshl_add_u64 v[250:251], v[122:123], 0, s[12:13]
	s_add_i32 m0, s98, 0x4000
	v_exp_f32_e32 v73, v73
	v_exp_f32_e32 v74, v74
	global_load_lds_dwordx4 v[250:251], off
	v_exp_f32_e32 v75, v75
	v_exp_f32_e32 v76, v76
	v_exp_f32_e32 v77, v77
	s_waitcnt lgkmcnt(1)
	v_mfma_f32_32x32x16_bf16 v[98:113], v[212:215], v[138:141], v[98:113]
	s_mov_b32 m0, s99
	v_exp_f32_e32 v78, v78
	v_exp_f32_e32 v79, v79
	v_lshl_add_u64 v[250:251], v[116:117], 0, s[40:41]
	global_load_lds_dwordx4 v[116:117], off
	s_add_i32 m0, s99, 0x2000
	v_exp_f32_e32 v80, v80
	v_exp_f32_e32 v81, v81
	v_add_u32_e32 v174, 0x2000, v203
	global_load_lds_dwordx4 v[250:251], off
	s_waitcnt lgkmcnt(0)
	v_mfma_f32_32x32x16_bf16 v[82:97], v[216:219], v[138:141], v[82:97]
	ds_read_b128 v[212:215], v126
	ds_read_b128 v[216:219], v126 offset:6144
	v_add_u32_e32 v126, s6, v205
	s_waitcnt lgkmcnt(1)
	v_mfma_f32_32x32x16_bf16 v[98:113], v[212:215], v[134:137], v[98:113]
	ds_read_b128 v[212:215], v126
	ds_read_b128 v[220:223], v126 offset:6144
	v_add_u32_e32 v126, s6, v206
	s_waitcnt lgkmcnt(2)
	v_mfma_f32_32x32x16_bf16 v[82:97], v[216:219], v[134:137], v[82:97]
	ds_read_b128 v[216:219], v126
	ds_read_b128 v[224:227], v126 offset:6144
	v_add_u32_e32 v126, s6, v207
	ds_read_b128 v[228:231], v126
	ds_read_b128 v[232:235], v126 offset:6144
	v_pk_add_f32 v[126:127], v[50:51], v[66:67]
	v_cvt_pk_bf16_f32 v50, v50, v51
	v_cvt_pk_bf16_f32 v51, v52, v53
	s_waitcnt lgkmcnt(5)
	v_mfma_f32_32x32x16_bf16 v[98:113], v[212:215], v[130:133], v[98:113]
	v_pk_add_f32 v[212:213], v[52:53], v[68:69]
	v_cvt_pk_bf16_f32 v52, v54, v55
	v_cvt_pk_bf16_f32 v53, v56, v57
	v_pk_add_f32 v[126:127], v[212:213], v[126:127]
	v_pk_add_f32 v[212:213], v[54:55], v[70:71]
	v_cvt_pk_bf16_f32 v54, v58, v59
	s_waitcnt lgkmcnt(4)
	v_mfma_f32_32x32x16_bf16 v[82:97], v[220:223], v[130:133], v[82:97]
	v_pk_add_f32 v[126:127], v[212:213], v[126:127]
	v_pk_add_f32 v[212:213], v[56:57], v[72:73]
	v_cvt_pk_bf16_f32 v55, v60, v61
	v_cvt_pk_bf16_f32 v56, v62, v63
	v_cvt_pk_bf16_f32 v57, v64, v65
	v_pk_add_f32 v[126:127], v[212:213], v[126:127]
	v_pk_add_f32 v[212:213], v[58:59], v[74:75]
	v_cvt_pk_bf16_f32 v58, v66, v67
	v_cvt_pk_bf16_f32 v59, v68, v69
	s_waitcnt lgkmcnt(3)
	v_mfma_f32_32x32x16_bf16 v[98:113], v[216:219], v[146:149], v[98:113]
	v_pk_add_f32 v[126:127], v[212:213], v[126:127]
	v_pk_add_f32 v[212:213], v[60:61], v[76:77]
	v_cvt_pk_bf16_f32 v60, v70, v71
	v_cvt_pk_bf16_f32 v61, v72, v73
	v_pk_add_f32 v[126:127], v[212:213], v[126:127]
	v_pk_add_f32 v[212:213], v[62:63], v[78:79]
	v_cvt_pk_bf16_f32 v62, v74, v75
	v_cvt_pk_bf16_f32 v63, v76, v77
	s_waitcnt lgkmcnt(2)
; DEVI void pv_both(f32x16& o0, f32x16& o1, int vb, bf16x8 pa0, bf16x8 pa1, bf16x8 pa2, bf16x8 pa3) {
;     const s16x4 a0 = tr_read<v_rd_off(0, 0, 0)>(vb), b0 = tr_read<v_rd_off(0, 0, 1)>(vb), a1 = tr_read<v_rd_off(0, 1, 0)>(vb), b1 = tr_read<v_rd_off(0, 1, 1)>(vb);
;     const s16x4 a2 = tr_read<v_rd_off(0, 2, 0)>(vb), b2 = tr_read<v_rd_off(0, 2, 1)>(vb), a3 = tr_read<v_rd_off(0, 3, 0)>(vb), b3 = tr_read<v_rd_off(0, 3, 1)>(vb);
;     const s16x4 c0 = tr_read<v_rd_off(1, 0, 0)>(vb), d0 = tr_read<v_rd_off(1, 0, 1)>(vb), c1 = tr_read<v_rd_off(1, 1, 0)>(vb), d1 = tr_read<v_rd_off(1, 1, 1)>(vb);
;     const s16x4 c2 = tr_read<v_rd_off(1, 2, 0)>(vb), d2 = tr_read<v_rd_off(1, 2, 1)>(vb), c3 = tr_read<v_rd_off(1, 3, 0)>(vb), d3 = tr_read<v_rd_off(1, 3, 1)>(vb);
;     asm volatile("s_waitcnt lgkmcnt(8)" ::: "memory"); SBAR();
;     ...
;     o0 = __builtin_amdgcn_mfma_f32_32x32x16_bf16(pa0, PK(a0, b0), o0, 0, 0, 0);
;     o0 = __builtin_amdgcn_mfma_f32_32x32x16_bf16(pa1, PK(a1, b1), o0, 0, 0, 0);
;     o0 = __builtin_amdgcn_mfma_f32_32x32x16_bf16(pa2, PK(a2, b2), o0, 0, 0, 0);
;     o0 = __builtin_amdgcn_mfma_f32_32x32x16_bf16(pa3, PK(a3, b3), o0, 0, 0, 0);
;     asm volatile("s_waitcnt lgkmcnt(0)" ::: "memory"); SBAR();
;     o1 = __builtin_amdgcn_mfma_f32_32x32x16_bf16(pa0, PK(c0, d0), o1, 0, 0, 0);
;     o1 = __builtin_amdgcn_mfma_f32_32x32x16_bf16(pa1, PK(c1, d1), o1, 0, 0, 0);
;     o1 = __builtin_amdgcn_mfma_f32_32x32x16_bf16(pa2, PK(c2, d2), o1, 0, 0, 0);
;     o1 = __builtin_amdgcn_mfma_f32_32x32x16_bf16(pa3, PK(c3, d3), o1, 0, 0, 0);
;     ...
; }
; template <bool FIRST> DEVI bool partialSM(f32x16& p0, f32x16& p1, float& m_reg, float& alpha) {
;     float pmax = p0[0];
; #pragma unroll
;     for (int r = 1; r < 16; ++r) pmax = fmaxf(pmax, p0[r]);
; #pragma unroll
;     for (int r = 0; r < 16; ++r) pmax = fmaxf(pmax, p1[r]);
;     { auto rr = __builtin_amdgcn_permlane32_swap(__float_as_uint(pmax), __float_as_uint(pmax), false, false);
;       pmax = fmaxf(__uint_as_float(rr[0]), __uint_as_float(rr[1])); }
;     if (FIRST) { m_reg = pmax; alpha = 1.f;
; #pragma unroll
;         for (int r = 0; r < 16; ++r) { p0[r] = __builtin_amdgcn_exp2f(p0[r] - pmax); p1[r] = p1[r] - pmax; }
;         return false;
;     } else if (__builtin_expect(__all(pmax <= ATT_THR), 1)) { alpha = 1.f;
; #pragma unroll
;         for (int r = 0; r < 16; ++r) p0[r] = __builtin_amdgcn_exp2f(p0[r]);
	v_mfma_f32_32x32x16_bf16 v[82:97], v[224:227], v[146:149], v[82:97]
	v_pk_add_f32 v[126:127], v[212:213], v[126:127]
	v_pk_add_f32 v[212:213], v[64:65], v[80:81]
	v_cvt_pk_bf16_f32 v64, v78, v79
	v_cvt_pk_bf16_f32 v65, v80, v81
	ds_read_b64_tr_b16 v[66:67], v174 offset:0
	ds_read_b64_tr_b16 v[68:69], v174 offset:0x400
	ds_read_b64_tr_b16 v[70:71], v174 offset:0x800
	ds_read_b64_tr_b16 v[72:73], v174 offset:0xc00
	ds_read_b64_tr_b16 v[74:75], v174 offset:0x1000
	ds_read_b64_tr_b16 v[76:77], v174 offset:0x1400
	ds_read_b64_tr_b16 v[78:79], v174 offset:0x1800
	ds_read_b64_tr_b16 v[80:81], v174 offset:0x1c00
	v_pk_add_f32 v[126:127], v[212:213], v[126:127]
	ds_read_b64_tr_b16 v[212:213], v174 offset:0x200
	ds_read_b64_tr_b16 v[214:215], v174 offset:0x600
	ds_read_b64_tr_b16 v[216:217], v174 offset:0xa00
	s_waitcnt lgkmcnt(12)
	v_mfma_f32_32x32x16_bf16 v[98:113], v[228:231], v[142:145], v[98:113]
	ds_read_b64_tr_b16 v[218:219], v174 offset:0xe00
	ds_read_b64_tr_b16 v[220:221], v174 offset:0x1200
	ds_read_b64_tr_b16 v[222:223], v174 offset:0x1600
	ds_read_b64_tr_b16 v[224:225], v174 offset:0x1a00
	ds_read_b64_tr_b16 v[226:227], v174 offset:0x1e00
	v_pk_add_f32 v[126:127], v[126:127], v[126:127] op_sel:[0,1] op_sel_hi:[1,0]
	s_waitcnt lgkmcnt(15)
	v_mfma_f32_32x32x16_bf16 v[82:97], v[232:235], v[142:145], v[82:97]
	v_mov_b32_e32 v127, v126
	s_nop 1
	v_permlane32_swap_b32_e32 v126, v127
	s_waitcnt lgkmcnt(14)
	v_mfma_f32_32x32x16_bf16 v[18:33], v[50:53], v[66:69], v[18:33]
	s_waitcnt lgkmcnt(12)
	v_mfma_f32_32x32x16_bf16 v[18:33], v[54:57], v[70:73], v[18:33]
	s_waitcnt lgkmcnt(10)
	v_mfma_f32_32x32x16_bf16 v[18:33], v[58:61], v[74:77], v[18:33]
	s_waitcnt lgkmcnt(8)
	v_mfma_f32_32x32x16_bf16 v[18:33], v[62:65], v[78:81], v[18:33]
	s_waitcnt lgkmcnt(6)
	v_mfma_f32_32x32x16_bf16 v[2:17], v[50:53], v[212:215], v[2:17]
	s_nop 0
	v_max_f32_e32 v249, v99, v99
	v_max_f32_e32 v250, v98, v98
	v_max_f32_e32 v249, v250, v249
	v_max3_f32 v249, v249, v100, v101
	v_max3_f32 v249, v249, v102, v103
	v_max3_f32 v251, v249, v104, v105
	v_max3_f32 v251, v251, v106, v107
	s_waitcnt lgkmcnt(4)
	v_exp_f32_e32 v50, v98
	v_exp_f32_e32 v51, v99
	v_exp_f32_e32 v52, v100
	v_exp_f32_e32 v53, v101
	v_mov_b64_e32 v[66:67], v[82:83]
	v_mov_b64_e32 v[68:69], v[84:85]
	v_mfma_f32_32x32x16_bf16 v[2:17], v[54:57], v[216:219], v[2:17]
	v_max3_f32 v251, v251, v108, v109
	v_max3_f32 v251, v251, v110, v111
	v_max3_f32 v251, v251, v112, v113
	v_max3_f32 v251, v251, v82, v83
	v_max3_f32 v251, v251, v84, v85
	v_max3_f32 v251, v251, v86, v87
	v_max3_f32 v251, v251, v88, v89
	s_waitcnt lgkmcnt(2)
	v_exp_f32_e32 v54, v102
	v_exp_f32_e32 v55, v103
	v_exp_f32_e32 v56, v104
	v_exp_f32_e32 v57, v105
	v_mov_b64_e32 v[70:71], v[86:87]
	v_mov_b64_e32 v[72:73], v[88:89]
	v_mfma_f32_32x32x16_bf16 v[2:17], v[58:61], v[220:223], v[2:17]
	v_max3_f32 v251, v251, v90, v91
	v_max3_f32 v251, v251, v92, v93
	v_max3_f32 v251, v251, v94, v95
	v_max3_f32 v251, v251, v96, v97
	v_mov_b32_e32 v252, v251
	s_nop 1
	v_permlane32_swap_b32_e32 v251, v252
	s_waitcnt lgkmcnt(0)
	v_exp_f32_e32 v58, v106
	v_exp_f32_e32 v59, v107
	v_exp_f32_e32 v60, v108
	v_exp_f32_e32 v61, v109
	v_mov_b64_e32 v[74:75], v[90:91]
	v_mov_b64_e32 v[76:77], v[92:93]
	v_mfma_f32_32x32x16_bf16 v[2:17], v[62:65], v[224:227], v[2:17]
	v_exp_f32_e32 v62, v110
	v_exp_f32_e32 v63, v111
	v_exp_f32_e32 v64, v112
	v_exp_f32_e32 v65, v113
	v_mov_b64_e32 v[78:79], v[94:95]
	v_mov_b64_e32 v[80:81], v[96:97]
	v_max_f32_e32 v252, v252, v252
	v_max_f32_e32 v251, v251, v251
	v_max_f32_e32 v174, v251, v252
	v_cmp_ge_f32_e32 vcc, s80, v174
	s_cmp_lg_u64 vcc, exec
	s_cselect_b64 s[6:7], -1, 0
	s_cbranch_scc1 .LBB0_2275
	v_mov_b32_e32 v203, 1.0
	v_mov_b32_e32 v204, v210
	s_branch .LBB0_2280

; DEVI unsigned cvt_pk_bf16(float lo, float hi) { unsigned r; asm volatile("v_cvt_pk_bf16_f32 %0, %1, %2" : "=v"(r) : "v"(lo), "v"(hi)); return r; }
; DEVI void cv_finish(char* img  , int lane, const CvRegs& R) {
;     if (!R.live) return;
;     const int n4 = (lane & 7) * 4, kq = lane >> 3;
;     const float sc = R.c.perm ? 16.f : 1.f;
; #pragma unroll
;     for (int c = 0; c < 4; ++c) { *(unsigned*)(img + (n4 + c) * 68 + (2 * kq) * 2) = cvt_pk_bf16(R.a0[c] * sc, R.b0[c] * sc); *(unsigned*)(img + (n4 + c) * 68 + (2 * kq + 16) * 2) = cvt_pk_bf16(R.a1[c] * sc, R.b1[c] * sc); }
;     asm volatile("" ::: "memory"); __builtin_amdgcn_wave_barrier();
.LBB0_2274:
	s_cmp_eq_u32 s95, 0
	s_cselect_b64 vcc, -1, 0
	s_waitcnt vmcnt(0)
	s_cbranch_scc0 .Lmy_cvs_b
	v_add_u32_e32 v84, v201, v202
	v_cvt_pk_bf16_f32 v83, v154, v158
	v_cvt_pk_bf16_f32 v85, v162, v166
	ds_write2_b32 v84, v83, v85 offset0:0 offset1:8
	v_cvt_pk_bf16_f32 v83, v155, v159
	v_cvt_pk_bf16_f32 v85, v163, v167
	ds_write2_b32 v84, v83, v85 offset0:17 offset1:25
	v_cvt_pk_bf16_f32 v83, v156, v160
	v_cvt_pk_bf16_f32 v85, v164, v168
	ds_write2_b32 v84, v83, v85 offset0:34 offset1:42
	v_cvt_pk_bf16_f32 v83, v157, v161
	v_cvt_pk_bf16_f32 v85, v165, v169
	ds_write2_b32 v84, v83, v85 offset0:51 offset1:59
	v_add_u32_e32 v84, v199, v200
	v_or_b32_e32 v90, v198, v196
	s_branch .Lmy_cvj_b
.Lmy_cvs_b:
	v_cndmask_b32_e64 v82, v186, 1.0, vcc
	v_mul_f32_e32 v83, v82, v154
	v_mul_f32_e32 v84, v82, v158
	v_cvt_pk_bf16_f32 v83, v83, v84
	v_add_u32_e32 v84, v201, v202
	ds_write_b32 v84, v83
	v_mul_f32_e32 v83, v82, v162
	v_mul_f32_e32 v85, v82, v166
	v_cvt_pk_bf16_f32 v83, v83, v85
	ds_write_b32 v84, v83 offset:32
	v_mul_f32_e32 v83, v82, v155
	v_mul_f32_e32 v85, v82, v159
	v_cvt_pk_bf16_f32 v83, v83, v85
	ds_write_b32 v84, v83 offset:68
	v_mul_f32_e32 v83, v82, v163
	v_mul_f32_e32 v85, v82, v167
	v_cvt_pk_bf16_f32 v83, v83, v85
	ds_write_b32 v84, v83 offset:100
	v_mul_f32_e32 v83, v82, v156
	v_mul_f32_e32 v85, v82, v160
	v_cvt_pk_bf16_f32 v83, v83, v85
	ds_write_b32 v84, v83 offset:136
	v_mul_f32_e32 v83, v82, v164
	v_mul_f32_e32 v85, v82, v168
	v_cvt_pk_bf16_f32 v83, v83, v85
	ds_write_b32 v84, v83 offset:168
	v_mul_f32_e32 v83, v82, v157
	v_mul_f32_e32 v85, v82, v161
	v_cvt_pk_bf16_f32 v83, v83, v85
	ds_write_b32 v84, v83 offset:204
	v_mul_f32_e32 v83, v82, v165
	v_mul_f32_e32 v82, v82, v169
	v_cndmask_b32_e32 v90, v197, v198, vcc
	v_cvt_pk_bf16_f32 v82, v83, v82
	ds_write_b32 v84, v82 offset:236
	v_add_u32_e32 v84, v199, v200
	v_or_b32_e32 v90, v90, v196
